# v37
# baseline (speedup 1.0000x reference)
.LBB0_10:
	s_or_b64 exec, exec, s[16:17]
	s_mov_b32 s3, 0xf4240
	v_cmp_gt_i32_e32 vcc, s3, v18
	s_waitcnt lgkmcnt(0)
	s_and_saveexec_b64 s[10:11], vcc
	s_cbranch_execz .LBB0_20
	v_mbcnt_lo_u32_b32 v1, -1, 0
	v_mbcnt_hi_u32_b32 v2, -1, v1
	v_and_b32_e32 v3, 64, v2
	v_xor_b32_e32 v1, 1, v2
	v_add_u32_e32 v3, 64, v3
	v_cmp_lt_i32_e32 vcc, v1, v3
	v_xor_b32_e32 v4, 2, v2
	s_lshl_b32 s24, s18, 11
	v_cndmask_b32_e32 v1, v2, v1, vcc
	v_cmp_lt_i32_e32 vcc, v4, v3
	s_add_i32 s14, s24, 0xfff80000
	v_ashrrev_i32_e32 v19, 31, v18
	v_cndmask_b32_e32 v4, v2, v4, vcc
	v_lshlrev_b32_e32 v24, 2, v4
	v_xor_b32_e32 v4, 4, v2
	v_cmp_lt_i32_e32 vcc, v4, v3
	s_lshl_b32 s25, s18, 12
	s_ashr_i32 s15, s14, 31
	v_cndmask_b32_e32 v4, v2, v4, vcc
	v_lshlrev_b32_e32 v25, 2, v4
	v_xor_b32_e32 v4, 8, v2
	v_cmp_lt_i32_e32 vcc, v4, v3
	v_lshlrev_b32_e32 v1, 2, v1
	s_add_i32 s24, s24, 0xfff00000
	v_cndmask_b32_e32 v2, v2, v4, vcc
	v_lshlrev_b32_e32 v26, 2, v2
	v_and_b32_e32 v2, 15, v0
	v_cmp_eq_u32_e64 s[6:7], 0, v2
	v_lshlrev_b32_e32 v2, 1, v0
	v_lshl_or_b32 v27, s2, 11, v2
	v_lshl_add_u64 v[2:3], v[18:19], 3, s[8:9]
	s_add_i32 s25, s25, 0xfff00000
	v_lshl_add_u64 v[20:21], v[2:3], 0, 4
	s_lshl_b64 s[16:17], s[14:15], 3
	s_lshl_b32 s15, s18, 10
	s_mov_b64 s[18:19], 0
	s_mov_b32 s26, 0x42fe0000
	s_movk_i32 s27, 0xff
	s_mov_b32 s28, 0xf423f
	s_branch .LBB0_13

_Z3k_BPKiS0_PiS1_PKfPDF16_:
	v_cmp_eq_u32_e32 vcc, 0, v0
	s_and_saveexec_b64 s[4:5], vcc
	v_mov_b32_e32 v2, 0
	v_mov_b32_e32 v3, v2
	ds_write_b64 v2, v[2:3] offset:27712
	s_or_b64 exec, exec, s[4:5]
	s_load_dwordx2 s[24:25], s[0:1], 0x0
	s_load_dwordx4 s[36:39], s[0:1], 0x20
	s_movk_i32 s3, 0x100
	v_cmp_gt_u32_e32 vcc, s3, v0
	v_mbcnt_lo_u32_b32 v16, -1, 0
	v_and_b32_e32 v14, 63, v0
	s_waitcnt lgkmcnt(0)
	s_barrier
	s_lshl_b32 s40, s2, 11
	s_add_i32 s40, s40, 0xf4240
	v_add_u32_e32 v60, s40, v0
	v_min_u32_e32 v61, 0x1869ff, v60
	v_lshlrev_b32_e32 v61, 5, v61
	global_load_dwordx4 v[28:31], v61, s[36:37]
	global_load_dwordx4 v[32:35], v61, s[36:37] offset:16
	v_add_u32_e32 v62, 0x400, v60
	v_min_u32_e32 v61, 0x1869ff, v62
	v_lshlrev_b32_e32 v61, 5, v61
	global_load_dwordx4 v[36:39], v61, s[36:37]
	global_load_dwordx4 v[40:43], v61, s[36:37] offset:16
	s_and_saveexec_b64 s[6:7], vcc
	s_cbranch_execz .LBB1_12
	s_load_dwordx2 s[4:5], s[0:1], 0x8
	s_lshl_b32 s3, s2, 8
	v_or_b32_e32 v2, s3, v0
	s_addk_i32 s3, 0x100
	v_ashrrev_i32_e32 v3, 31, v2
	v_or_b32_e32 v4, s3, v0
	s_waitcnt lgkmcnt(0)
	v_lshl_add_u64 v[2:3], v[2:3], 2, s[4:5]
	v_ashrrev_i32_e32 v5, 31, v4
	v_lshl_add_u64 v[4:5], v[4:5], 2, s[4:5]
	global_load_dword v1, v[2:3], off
	global_load_dword v6, v[4:5], off
	v_mbcnt_hi_u32_b32 v2, -1, v16
	v_and_b32_e32 v3, 64, v2
	v_xor_b32_e32 v4, 32, v2
	v_add_u32_e32 v3, 64, v3
	v_cmp_lt_i32_e64 s[4:5], v4, v3
	v_xor_b32_e32 v7, 16, v2
	v_xor_b32_e32 v8, 8, v2
	v_cndmask_b32_e64 v4, v2, v4, s[4:5]
	v_lshlrev_b32_e32 v4, 2, v4
	v_cmp_lt_i32_e64 s[4:5], v7, v3
	v_xor_b32_e32 v9, 4, v2
	v_xor_b32_e32 v10, 2, v2
	v_cndmask_b32_e64 v7, v2, v7, s[4:5]
	v_lshlrev_b32_e32 v7, 2, v7
	v_cmp_lt_i32_e64 s[4:5], v8, v3
	v_xor_b32_e32 v11, 1, v2
	s_movk_i32 s3, 0x1870
	v_cndmask_b32_e64 v8, v2, v8, s[4:5]
	v_lshlrev_b32_e32 v8, 2, v8
	v_cmp_lt_i32_e64 s[4:5], v9, v3
	v_lshlrev_b32_e32 v5, 2, v0
	s_waitcnt vmcnt(1)
	ds_bpermute_b32 v12, v4, v1
	s_waitcnt vmcnt(0)
	v_sub_u32_e32 v6, v6, v1
	ds_bpermute_b32 v4, v4, v6
	v_cndmask_b32_e64 v9, v2, v9, s[4:5]
	v_lshlrev_b32_e32 v9, 2, v9
	s_waitcnt lgkmcnt(1)
	v_add_u32_e32 v12, v12, v1
	ds_bpermute_b32 v13, v7, v12
	s_waitcnt lgkmcnt(1)
	v_add_u32_e32 v4, v4, v6
	ds_bpermute_b32 v7, v7, v4
	v_cmp_lt_i32_e64 s[4:5], v10, v3
	s_waitcnt lgkmcnt(1)
	v_add_u32_e32 v12, v13, v12
	v_cndmask_b32_e64 v10, v2, v10, s[4:5]
	s_waitcnt lgkmcnt(0)
	v_add_u32_e32 v4, v7, v4
	ds_bpermute_b32 v7, v8, v12
	ds_bpermute_b32 v8, v8, v4
	v_lshlrev_b32_e32 v10, 2, v10
	v_cmp_lt_i32_e64 s[4:5], v11, v3
	s_waitcnt lgkmcnt(1)
	v_add_u32_e32 v7, v7, v12
	s_waitcnt lgkmcnt(0)
	v_add_u32_e32 v4, v8, v4
	ds_bpermute_b32 v8, v9, v7
	ds_bpermute_b32 v9, v9, v4
	v_cndmask_b32_e64 v2, v2, v11, s[4:5]
	v_lshlrev_b32_e32 v2, 2, v2
	v_cmp_eq_u32_e64 s[4:5], 0, v14
	s_waitcnt lgkmcnt(1)
	v_add_u32_e32 v7, v8, v7
	s_waitcnt lgkmcnt(0)
	v_add_u32_e32 v4, v9, v4
	ds_bpermute_b32 v8, v10, v7
	ds_bpermute_b32 v9, v10, v4
	v_mad_u32_u24 v10, v0, s3, v1
	ds_write2st64_b32 v5, v6, v10 offset0:96 offset1:100
	v_mov_b32_e32 v6, 0
	s_waitcnt lgkmcnt(2)
	v_add_u32_e32 v3, v8, v7
	s_waitcnt lgkmcnt(1)
	v_add_u32_e32 v1, v9, v4
	ds_bpermute_b32 v4, v2, v3
	ds_bpermute_b32 v2, v2, v1
	ds_write_b32 v5, v6 offset:26624
	s_and_b64 exec, exec, s[4:5]
	s_cbranch_execz .LBB1_12
	s_mov_b64 s[4:5], exec
	s_waitcnt lgkmcnt(2)
	v_add_u32_e32 v3, v4, v3
	s_mov_b32 s8, 0
